# v74 plus first K-loop iteration peeled (C=0 on first MFMAs, no accumulator zeroing) in the in-proj and FFN gate/up GEMMs
# speedup vs baseline: 1.0066x; 1.0049x over previous
.LBB0_1603:
	v_mov_b64_e32 v[2:3], 0xb00
	v_cmp_lt_i64_e32 vcc, s[4:5], v[2:3]
	v_readlane_b32 s4, v252, 12
	v_readlane_b32 s5, v252, 13
	s_add_u32 s4, s4, s37
	s_addc_u32 s5, s5, 0
	s_and_b64 s[6:7], vcc, exec
	v_readlane_b32 s6, v251, 16
	s_cselect_b32 s42, s5, s3
	s_cselect_b32 s46, s4, s2
	v_readlane_b32 s7, v251, 17
	s_add_u32 s6, s6, s36
	s_addc_u32 s7, s7, 0
	s_and_b64 s[10:11], vcc, exec
	s_cselect_b32 s47, s7, s9
	s_cselect_b32 s48, s6, s8
	s_add_u32 s2, s2, 0x40080
	s_addc_u32 s3, s3, 0
	s_add_u32 s49, s8, 0x100
	s_addc_u32 s50, s9, 0
	s_mov_b32 s51, -2
	s_add_u32 s8, s2, 0xfffc0080
	s_addc_u32 s9, s3, -1
	s_add_i32 s52, 0, 0x10000
	v_add_u32_e32 v142, s52, v159
	ds_read_b128 v[130:133], v142
	ds_read_b128 v[134:137], v142 offset:1024
	ds_read_b128 v[138:141], v142 offset:2048
	ds_read_b128 v[142:145], v142 offset:3072
	s_cmp_eq_u32 s51, 12
	s_cselect_b32 s11, s42, s9
	s_cselect_b32 s10, s46, s8
	s_cselect_b32 s9, s47, s50
	s_cselect_b32 s8, s48, s49
	v_lshl_add_u64 v[160:161], s[2:3], 0, v[152:153]
	s_add_i32 m0, s16, 0xc000
	ds_read_b128 v[166:169], v165
	ds_read_b128 v[170:173], v165 offset:1024
	ds_read_b128 v[174:177], v165 offset:2048
	ds_read_b128 v[178:181], v165 offset:3072
	ds_read_b128 v[182:185], v165 offset:4096
	ds_read_b128 v[196:199], v165 offset:5120
	ds_read_b128 v[200:203], v165 offset:6144
	ds_read_b128 v[204:207], v165 offset:7168
	global_load_lds_dwordx4 v[160:161], off
	v_lshl_add_u64 v[160:161], s[2:3], 0, v[154:155]
	s_add_i32 m0, s16, 0xe000
	s_nop 0
	global_load_lds_dwordx4 v[160:161], off
	s_waitcnt lgkmcnt(8)
	s_barrier
	s_waitcnt lgkmcnt(0)
	s_setprio 1
	s_waitcnt lgkmcnt(0)
	v_mfma_f32_16x16x32_bf16 v[126:129], v[130:133], v[166:169], 0
	v_mfma_f32_16x16x32_bf16 v[118:121], v[138:141], v[166:169], 0
	v_mfma_f32_16x16x32_bf16 v[110:113], v[130:133], v[174:177], 0
	v_mfma_f32_16x16x32_bf16 v[102:105], v[138:141], v[174:177], 0
	v_mfma_f32_16x16x32_bf16 v[94:97], v[130:133], v[182:185], 0
	v_mfma_f32_16x16x32_bf16 v[86:89], v[138:141], v[182:185], 0
	v_mfma_f32_16x16x32_bf16 v[78:81], v[130:133], v[200:203], 0
	v_mfma_f32_16x16x32_bf16 v[70:73], v[138:141], v[200:203], 0
	v_mfma_f32_16x16x32_bf16 v[126:129], v[134:137], v[170:173], v[126:129]
	v_mfma_f32_16x16x32_bf16 v[118:121], v[142:145], v[170:173], v[118:121]
	v_mfma_f32_16x16x32_bf16 v[110:113], v[134:137], v[178:181], v[110:113]
	v_mfma_f32_16x16x32_bf16 v[102:105], v[142:145], v[178:181], v[102:105]
	v_mfma_f32_16x16x32_bf16 v[94:97], v[134:137], v[196:199], v[94:97]
	v_mfma_f32_16x16x32_bf16 v[86:89], v[142:145], v[196:199], v[86:89]
	v_mfma_f32_16x16x32_bf16 v[78:81], v[134:137], v[204:207], v[78:81]
	v_mfma_f32_16x16x32_bf16 v[70:73], v[142:145], v[204:207], v[70:73]
	s_setprio 0
	s_barrier
	s_add_i32 s54, 0, 0x14000
	s_add_i32 s52, s52, s14
	v_add_u32_e32 v156, s54, v159
	v_lshl_add_u64 v[160:161], s[8:9], 0, v[0:1]
	s_mov_b32 m0, s52
	ds_read_b128 v[208:211], v156
	ds_read_b128 v[212:215], v156 offset:1024
	ds_read_b128 v[216:219], v156 offset:2048
	ds_read_b128 v[220:223], v156 offset:3072
	global_load_lds_dwordx4 v[160:161], off
	v_lshl_add_u64 v[192:193], s[8:9], 0, v[146:147]
	s_add_i32 m0, s52, 0x2000
	s_nop 0
	global_load_lds_dwordx4 v[192:193], off
	s_barrier
	s_waitcnt lgkmcnt(0)
	s_setprio 1
	s_waitcnt lgkmcnt(0)
	v_mfma_f32_16x16x32_bf16 v[122:125], v[208:211], v[166:169], 0
	v_mfma_f32_16x16x32_bf16 v[114:117], v[216:219], v[166:169], 0
	v_mfma_f32_16x16x32_bf16 v[106:109], v[208:211], v[174:177], 0
	v_mfma_f32_16x16x32_bf16 v[98:101], v[216:219], v[174:177], 0
	v_mfma_f32_16x16x32_bf16 v[90:93], v[208:211], v[182:185], 0
	v_mfma_f32_16x16x32_bf16 v[82:85], v[216:219], v[182:185], 0
	v_mfma_f32_16x16x32_bf16 v[74:77], v[208:211], v[200:203], 0
	v_mfma_f32_16x16x32_bf16 v[66:69], v[216:219], v[200:203], 0
	v_mfma_f32_16x16x32_bf16 v[122:125], v[212:215], v[170:173], v[122:125]
	v_mfma_f32_16x16x32_bf16 v[114:117], v[220:223], v[170:173], v[114:117]
	v_mfma_f32_16x16x32_bf16 v[106:109], v[212:215], v[178:181], v[106:109]
	v_mfma_f32_16x16x32_bf16 v[98:101], v[220:223], v[178:181], v[98:101]
	v_mfma_f32_16x16x32_bf16 v[90:93], v[212:215], v[196:199], v[90:93]
	v_mfma_f32_16x16x32_bf16 v[82:85], v[220:223], v[196:199], v[82:85]
	v_mfma_f32_16x16x32_bf16 v[74:77], v[212:215], v[204:207], v[74:77]
	v_mfma_f32_16x16x32_bf16 v[66:69], v[220:223], v[204:207], v[66:69]
	s_setprio 0
	s_mov_b32 m0, s16
	v_lshl_add_u64 v[224:225], s[10:11], 0, v[150:151]
	s_barrier
	ds_read_b128 v[166:169], v165 offset:16384
	ds_read_b128 v[170:173], v165 offset:17408
	ds_read_b128 v[174:177], v165 offset:18432
	ds_read_b128 v[178:181], v165 offset:19456
	ds_read_b128 v[182:185], v165 offset:20480
	ds_read_b128 v[196:199], v165 offset:21504
	ds_read_b128 v[200:203], v165 offset:22528
	ds_read_b128 v[204:207], v165 offset:23552
	global_load_lds_dwordx4 v[224:225], off
	v_lshl_add_u64 v[226:227], s[10:11], 0, v[148:149]
	s_mov_b32 m0, s17
	s_nop 0
	global_load_lds_dwordx4 v[226:227], off
	s_barrier
	s_waitcnt lgkmcnt(0)
	s_setprio 1
	s_waitcnt lgkmcnt(0)
	v_mfma_f32_16x16x32_bf16 v[62:65], v[130:133], v[166:169], 0
	v_mfma_f32_16x16x32_bf16 v[54:57], v[138:141], v[166:169], 0
	v_mfma_f32_16x16x32_bf16 v[46:49], v[130:133], v[174:177], 0
	v_mfma_f32_16x16x32_bf16 v[38:41], v[138:141], v[174:177], 0
	v_mfma_f32_16x16x32_bf16 v[30:33], v[130:133], v[182:185], 0
	v_mfma_f32_16x16x32_bf16 v[22:25], v[138:141], v[182:185], 0
	v_mfma_f32_16x16x32_bf16 v[14:17], v[130:133], v[200:203], 0
	v_mfma_f32_16x16x32_bf16 v[6:9], v[138:141], v[200:203], 0
	v_mfma_f32_16x16x32_bf16 v[62:65], v[134:137], v[170:173], v[62:65]
	v_mfma_f32_16x16x32_bf16 v[54:57], v[142:145], v[170:173], v[54:57]
	v_mfma_f32_16x16x32_bf16 v[46:49], v[134:137], v[178:181], v[46:49]
	v_mfma_f32_16x16x32_bf16 v[38:41], v[142:145], v[178:181], v[38:41]
	v_mfma_f32_16x16x32_bf16 v[30:33], v[134:137], v[196:199], v[30:33]
	v_mfma_f32_16x16x32_bf16 v[22:25], v[142:145], v[196:199], v[22:25]
	v_mfma_f32_16x16x32_bf16 v[14:17], v[134:137], v[204:207], v[14:17]
	v_mfma_f32_16x16x32_bf16 v[6:9], v[142:145], v[204:207], v[6:9]
	s_setprio 0
	s_barrier
	s_add_u32 s52, s8, 0x40000
	s_addc_u32 s53, s9, 0
	s_add_i32 s54, s54, s14
	v_lshl_add_u64 v[130:131], s[52:53], 0, v[0:1]
	s_mov_b32 m0, s54
	s_nop 0
	global_load_lds_dwordx4 v[130:131], off
	v_lshl_add_u64 v[130:131], s[52:53], 0, v[146:147]
	s_add_i32 m0, s54, 0x2000
	s_nop 0
	global_load_lds_dwordx4 v[130:131], off
	s_waitcnt vmcnt(6)
	s_barrier
	s_setprio 1
	v_mfma_f32_16x16x32_bf16 v[58:61], v[208:211], v[166:169], 0
	v_mfma_f32_16x16x32_bf16 v[50:53], v[216:219], v[166:169], 0
	v_mfma_f32_16x16x32_bf16 v[42:45], v[208:211], v[174:177], 0
	v_mfma_f32_16x16x32_bf16 v[34:37], v[216:219], v[174:177], 0
	v_mfma_f32_16x16x32_bf16 v[26:29], v[208:211], v[182:185], 0
	v_mfma_f32_16x16x32_bf16 v[18:21], v[216:219], v[182:185], 0
	v_mfma_f32_16x16x32_bf16 v[10:13], v[208:211], v[200:203], 0
	v_mfma_f32_16x16x32_bf16 v[2:5], v[216:219], v[200:203], 0
	v_mfma_f32_16x16x32_bf16 v[58:61], v[212:215], v[170:173], v[58:61]
	v_mfma_f32_16x16x32_bf16 v[50:53], v[220:223], v[170:173], v[50:53]
	v_mfma_f32_16x16x32_bf16 v[42:45], v[212:215], v[178:181], v[42:45]
	v_mfma_f32_16x16x32_bf16 v[34:37], v[220:223], v[178:181], v[34:37]
	v_mfma_f32_16x16x32_bf16 v[26:29], v[212:215], v[196:199], v[26:29]
	v_mfma_f32_16x16x32_bf16 v[18:21], v[220:223], v[196:199], v[18:21]
	v_mfma_f32_16x16x32_bf16 v[10:13], v[212:215], v[204:207], v[10:13]
	v_mfma_f32_16x16x32_bf16 v[2:5], v[220:223], v[204:207], v[2:5]
	s_setprio 0
	s_add_i32 s52, 0, 0x18000
	v_add_u32_e32 v142, s52, v159
	s_barrier
	ds_read_b128 v[130:133], v142
	ds_read_b128 v[134:137], v142 offset:1024
	ds_read_b128 v[138:141], v142 offset:2048
	ds_read_b128 v[142:145], v142 offset:3072
	s_add_u32 s10, s10, 0x40000
	s_addc_u32 s11, s11, 0
	s_mov_b32 m0, s20
	v_lshl_add_u64 v[208:209], s[10:11], 0, v[150:151]
	ds_read_b128 v[166:169], v165 offset:32768
	ds_read_b128 v[170:173], v165 offset:33792
	ds_read_b128 v[174:177], v165 offset:34816
	ds_read_b128 v[178:181], v165 offset:35840
	ds_read_b128 v[182:185], v165 offset:36864
	ds_read_b128 v[196:199], v165 offset:37888
	ds_read_b128 v[200:203], v165 offset:38912
	ds_read_b128 v[204:207], v165 offset:39936
	global_load_lds_dwordx4 v[208:209], off
	v_lshl_add_u64 v[208:209], s[10:11], 0, v[148:149]
	s_mov_b32 m0, s21
	s_nop 0
	global_load_lds_dwordx4 v[208:209], off
	s_waitcnt lgkmcnt(8)
	s_barrier
	s_waitcnt lgkmcnt(0)
	s_setprio 1
	s_waitcnt lgkmcnt(0)
	v_mfma_f32_16x16x32_bf16 v[126:129], v[130:133], v[166:169], v[126:129]
	v_mfma_f32_16x16x32_bf16 v[118:121], v[138:141], v[166:169], v[118:121]
	v_mfma_f32_16x16x32_bf16 v[110:113], v[130:133], v[174:177], v[110:113]
	v_mfma_f32_16x16x32_bf16 v[102:105], v[138:141], v[174:177], v[102:105]
	v_mfma_f32_16x16x32_bf16 v[94:97], v[130:133], v[182:185], v[94:97]
	v_mfma_f32_16x16x32_bf16 v[86:89], v[138:141], v[182:185], v[86:89]
	v_mfma_f32_16x16x32_bf16 v[78:81], v[130:133], v[200:203], v[78:81]
	v_mfma_f32_16x16x32_bf16 v[70:73], v[138:141], v[200:203], v[70:73]
	v_mfma_f32_16x16x32_bf16 v[126:129], v[134:137], v[170:173], v[126:129]
	v_mfma_f32_16x16x32_bf16 v[118:121], v[142:145], v[170:173], v[118:121]
	v_mfma_f32_16x16x32_bf16 v[110:113], v[134:137], v[178:181], v[110:113]
	v_mfma_f32_16x16x32_bf16 v[102:105], v[142:145], v[178:181], v[102:105]
	v_mfma_f32_16x16x32_bf16 v[94:97], v[134:137], v[196:199], v[94:97]
	v_mfma_f32_16x16x32_bf16 v[86:89], v[142:145], v[196:199], v[86:89]
	v_mfma_f32_16x16x32_bf16 v[78:81], v[134:137], v[204:207], v[78:81]
	v_mfma_f32_16x16x32_bf16 v[70:73], v[142:145], v[204:207], v[70:73]
	s_setprio 0
	s_barrier
	s_add_i32 s10, 0, 0x1c000
	s_add_i32 s11, s52, s14
	v_add_u32_e32 v156, s10, v159
	v_lshl_add_u64 v[160:161], v[160:161], 0, s[44:45]
	s_mov_b32 m0, s11
	ds_read_b128 v[208:211], v156
	ds_read_b128 v[212:215], v156 offset:1024
	ds_read_b128 v[216:219], v156 offset:2048
	ds_read_b128 v[220:223], v156 offset:3072
	global_load_lds_dwordx4 v[160:161], off
	v_lshl_add_u64 v[160:161], v[192:193], 0, s[44:45]
	s_add_i32 m0, s11, 0x2000
	s_nop 0
	global_load_lds_dwordx4 v[160:161], off
	s_barrier
	s_waitcnt lgkmcnt(0)
	s_setprio 1
	s_waitcnt lgkmcnt(0)
	v_mfma_f32_16x16x32_bf16 v[122:125], v[208:211], v[166:169], v[122:125]
	v_mfma_f32_16x16x32_bf16 v[114:117], v[216:219], v[166:169], v[114:117]
	v_mfma_f32_16x16x32_bf16 v[106:109], v[208:211], v[174:177], v[106:109]
	v_mfma_f32_16x16x32_bf16 v[98:101], v[216:219], v[174:177], v[98:101]
	v_mfma_f32_16x16x32_bf16 v[90:93], v[208:211], v[182:185], v[90:93]
	v_mfma_f32_16x16x32_bf16 v[82:85], v[216:219], v[182:185], v[82:85]
	v_mfma_f32_16x16x32_bf16 v[74:77], v[208:211], v[200:203], v[74:77]
	v_mfma_f32_16x16x32_bf16 v[66:69], v[216:219], v[200:203], v[66:69]
	v_mfma_f32_16x16x32_bf16 v[122:125], v[212:215], v[170:173], v[122:125]
	v_mfma_f32_16x16x32_bf16 v[114:117], v[220:223], v[170:173], v[114:117]
	v_mfma_f32_16x16x32_bf16 v[106:109], v[212:215], v[178:181], v[106:109]
	v_mfma_f32_16x16x32_bf16 v[98:101], v[220:223], v[178:181], v[98:101]
	v_mfma_f32_16x16x32_bf16 v[90:93], v[212:215], v[196:199], v[90:93]
	v_mfma_f32_16x16x32_bf16 v[82:85], v[220:223], v[196:199], v[82:85]
	v_mfma_f32_16x16x32_bf16 v[74:77], v[212:215], v[204:207], v[74:77]
	v_mfma_f32_16x16x32_bf16 v[66:69], v[220:223], v[204:207], v[66:69]
	s_setprio 0
	s_mov_b32 m0, s26
	v_lshl_add_u64 v[160:161], v[224:225], 0, s[44:45]
	s_barrier
	ds_read_b128 v[166:169], v165 offset:49152
	ds_read_b128 v[170:173], v165 offset:50176
	ds_read_b128 v[174:177], v165 offset:51200
	ds_read_b128 v[178:181], v165 offset:52224
	ds_read_b128 v[182:185], v165 offset:53248
	ds_read_b128 v[196:199], v165 offset:54272
	ds_read_b128 v[200:203], v165 offset:55296
	ds_read_b128 v[204:207], v165 offset:56320
	global_load_lds_dwordx4 v[160:161], off
	v_lshl_add_u64 v[160:161], v[226:227], 0, s[44:45]
	s_mov_b32 m0, s27
	s_nop 0
	global_load_lds_dwordx4 v[160:161], off
	s_barrier
	s_waitcnt lgkmcnt(0)
	s_setprio 1
	s_waitcnt lgkmcnt(0)
	v_mfma_f32_16x16x32_bf16 v[62:65], v[130:133], v[166:169], v[62:65]
	v_mfma_f32_16x16x32_bf16 v[54:57], v[138:141], v[166:169], v[54:57]
	v_mfma_f32_16x16x32_bf16 v[46:49], v[130:133], v[174:177], v[46:49]
	v_mfma_f32_16x16x32_bf16 v[38:41], v[138:141], v[174:177], v[38:41]
	v_mfma_f32_16x16x32_bf16 v[30:33], v[130:133], v[182:185], v[30:33]
	v_mfma_f32_16x16x32_bf16 v[22:25], v[138:141], v[182:185], v[22:25]
	v_mfma_f32_16x16x32_bf16 v[14:17], v[130:133], v[200:203], v[14:17]
	v_mfma_f32_16x16x32_bf16 v[6:9], v[138:141], v[200:203], v[6:9]
	v_mfma_f32_16x16x32_bf16 v[62:65], v[134:137], v[170:173], v[62:65]
	v_mfma_f32_16x16x32_bf16 v[54:57], v[142:145], v[170:173], v[54:57]
	v_mfma_f32_16x16x32_bf16 v[46:49], v[134:137], v[178:181], v[46:49]
	v_mfma_f32_16x16x32_bf16 v[38:41], v[142:145], v[178:181], v[38:41]
	v_mfma_f32_16x16x32_bf16 v[30:33], v[134:137], v[196:199], v[30:33]
	v_mfma_f32_16x16x32_bf16 v[22:25], v[142:145], v[196:199], v[22:25]
	v_mfma_f32_16x16x32_bf16 v[14:17], v[134:137], v[204:207], v[14:17]
	v_mfma_f32_16x16x32_bf16 v[6:9], v[142:145], v[204:207], v[6:9]
	s_setprio 0
	s_barrier
	s_add_u32 s8, s8, 0x40080
	s_addc_u32 s9, s9, 0
	s_add_i32 s10, s10, s14
	v_lshl_add_u64 v[130:131], s[8:9], 0, v[0:1]
	s_mov_b32 m0, s10
	s_nop 0
	global_load_lds_dwordx4 v[130:131], off
	v_lshl_add_u64 v[130:131], s[8:9], 0, v[146:147]
	s_add_i32 m0, s10, 0x2000
	s_nop 0
	global_load_lds_dwordx4 v[130:131], off
	s_waitcnt vmcnt(6)
	s_barrier
	s_setprio 1
	v_mfma_f32_16x16x32_bf16 v[58:61], v[208:211], v[166:169], v[58:61]
	v_mfma_f32_16x16x32_bf16 v[50:53], v[216:219], v[166:169], v[50:53]
	v_mfma_f32_16x16x32_bf16 v[42:45], v[208:211], v[174:177], v[42:45]
	v_mfma_f32_16x16x32_bf16 v[34:37], v[216:219], v[174:177], v[34:37]
	v_mfma_f32_16x16x32_bf16 v[26:29], v[208:211], v[182:185], v[26:29]
	v_mfma_f32_16x16x32_bf16 v[18:21], v[216:219], v[182:185], v[18:21]
	v_mfma_f32_16x16x32_bf16 v[10:13], v[208:211], v[200:203], v[10:13]
	v_mfma_f32_16x16x32_bf16 v[2:5], v[216:219], v[200:203], v[2:5]
	v_mfma_f32_16x16x32_bf16 v[58:61], v[212:215], v[170:173], v[58:61]
	v_mfma_f32_16x16x32_bf16 v[50:53], v[220:223], v[170:173], v[50:53]
	v_mfma_f32_16x16x32_bf16 v[42:45], v[212:215], v[178:181], v[42:45]
	v_mfma_f32_16x16x32_bf16 v[34:37], v[220:223], v[178:181], v[34:37]
	v_mfma_f32_16x16x32_bf16 v[26:29], v[212:215], v[196:199], v[26:29]
	v_mfma_f32_16x16x32_bf16 v[18:21], v[220:223], v[196:199], v[18:21]
	v_mfma_f32_16x16x32_bf16 v[10:13], v[212:215], v[204:207], v[10:13]
	v_mfma_f32_16x16x32_bf16 v[2:5], v[220:223], v[204:207], v[2:5]
	s_setprio 0
	s_add_i32 s51, s51, 2
	s_add_u32 s2, s2, 0x100
	s_addc_u32 s3, s3, 0
	s_add_u32 s49, s49, 0x100
	s_addc_u32 s50, s50, 0
	s_cmp_gt_u32 s51, 13
	s_barrier
